# attention: s_setprio 1/0 around the QK and PV MFMA blocks (MFMA wave gets issue priority over softmax wave)
# baseline (speedup 1.0000x reference)
; #define LAS __attribute__((address_space(3)))
; #define SBAR() __builtin_amdgcn_sched_barrier(0)
; __device__ __forceinline__ void qkt(f32x16& p0, f32x16& p1, LAS unsigned char* lds  , int r32, int hi, const bf16x8* qr) {
;     p0 = f32x16{}; p1 = f32x16{};
;     const LAS unsigned char* kb[4];
; #pragma unroll
;     for (int dd = 0; dd < 4; ++dd) kb[dd] = lds + K_OFF + KSWZ(r32, (dd * 16 + hi * 8) * 2);
; #pragma unroll
;     for (int d0 = 0; d0 < 8; ++d0) { const LAS unsigned char* a = kb[d0 & 3] + (d0 >> 2) * 128;
;         const bf16x8 b0 = *(const LAS bf16x8*)(a);
;         const bf16x8 b1 = *(const LAS bf16x8*)(a + 32 * 256);
;         p0 = __builtin_amdgcn_mfma_f32_32x32x16_bf16(b0, qr[d0], p0, 0, 0, 0);
;         p1 = __builtin_amdgcn_mfma_f32_32x32x16_bf16(b1, qr[d0], p1, 0, 0, 0); }
; #pragma unroll
;     for (int e = 0; e < 4; ++e) { const LAS unsigned char* a = lds + P_OFF + KPSWZ(r32, (e * 2 + hi) * 16);
;         const bf16x8 b0 = *(const LAS bf16x8*)(a);
;         const bf16x8 b1 = *(const LAS bf16x8*)(a + 32 * 128);
;         p0 = __builtin_amdgcn_mfma_f32_32x32x16_bf16(b0, qr[8 + e], p0, 0, 0, 0);
;         p1 = __builtin_amdgcn_mfma_f32_32x32x16_bf16(b1, qr[8 + e], p1, 0, 0, 0); }
; }
; __device__ __forceinline__ void attn_unit(LAS unsigned char* lds, int b, int h, int qb, const bf16* Q  , const bf16* KV  , const bf16* KPE  ,
;                                           const float* ROPE  , bf16* O  , const int wave_) {
;     ...
;     for (int t = 0; t < NT; ++t) {
;         asm volatile("s_waitcnt vmcnt(5)" ::: "memory"); __builtin_amdgcn_s_barrier();
;         { const int tn = (t + 2 < NT) ? t + 2 : NT - 1; AISSUE(tn, bl); }
;         const int kb_ = t * KVBLK;
;         if (kb_ <= qlo + 31) {
;             SBAR(); qkt(p0, p1, lds + bc, r32, hi, qr);
;             if (kb_ + KVBLK - 1 > qlo) mask_tile(p0, p1, qm - kb_);
.LBB0_720:
	s_add_i32 s4, s73, 2
	s_min_u32 s70, s4, s2
	s_lshl_b64 s[4:5], s[70:71], 18
	s_add_u32 s4, s96, s4
	s_addc_u32 s5, s97, s5
	v_lshl_add_u64 v[64:65], v[150:151], 1, s[4:5]
	s_add_i32 s8, s95, s69
	v_lshl_add_u64 v[64:65], v[64:65], 0, s[66:67]
	s_mov_b32 m0, s8
	s_waitcnt vmcnt(5)
	s_barrier
	global_load_lds_dwordx4 v[64:65], off
	v_lshl_add_u64 v[64:65], v[152:153], 1, s[4:5]
	v_lshl_add_u64 v[64:65], v[64:65], 0, s[66:67]
	s_add_i32 m0, s8, 0x2000
	s_lshl_b64 s[6:7], s[70:71], 13
	global_load_lds_dwordx4 v[64:65], off
	v_lshl_add_u64 v[64:65], v[146:147], 1, s[4:5]
	s_add_i32 m0, s8, 0x4000
	s_nop 0
	global_load_lds_dwordx4 v[64:65], off
	v_lshl_add_u64 v[64:65], v[148:149], 1, s[4:5]
	s_add_i32 m0, s8, 0x6000
	s_sub_i32 s4, s94, 63
	global_load_lds_dwordx4 v[64:65], off
	v_lshl_add_u64 v[64:65], v[154:155], 0, s[6:7]
	s_add_i32 m0, s8, 0x8000
	s_cmp_gt_i32 s4, s68
	global_load_lds_dwordx4 v[64:65], off
	s_cbranch_scc1 .LBB0_728
	s_add_i32 s4, s72, 0
	v_add_u32_e32 v216, s4, v160
	v_add_u32_e32 v220, s4, v166
	v_add_u32_e32 v217, v216, v162
	v_add_u32_e32 v218, v216, v163
	v_add_u32_e32 v219, v216, v165
	v_add_u32_e32 v216, v216, v161
	v_add_u32_e32 v221, v220, v168
	v_add_u32_e32 v222, v220, v169
	v_add_u32_e32 v223, v220, v170
	v_add_u32_e32 v220, v220, v167
	ds_read_b128 v[176:179], v216 offset:16384
	ds_read_b128 v[180:183], v216 offset:24576
	ds_read_b128 v[184:187], v217 offset:16384
	ds_read_b128 v[188:191], v217 offset:24576
	ds_read_b128 v[192:195], v218 offset:16384
	ds_read_b128 v[196:199], v218 offset:24576
	ds_read_b128 v[200:203], v219 offset:16384
	ds_read_b128 v[204:207], v219 offset:24576
	s_cmp_le_i32 s94, s33
	ds_read_b128 v[208:211], v216 offset:16512
	ds_read_b128 v[212:215], v216 offset:24704
	s_waitcnt lgkmcnt(8)
	s_setprio 1
	v_mfma_f32_32x32x16_bf16 v[80:95], v[176:179], v[124:127], 0
	v_mfma_f32_32x32x16_bf16 v[64:79], v[180:183], v[124:127], 0
	ds_read_b128 v[176:179], v217 offset:16512
	ds_read_b128 v[180:183], v217 offset:24704
	s_waitcnt lgkmcnt(8)
	v_mfma_f32_32x32x16_bf16 v[80:95], v[184:187], v[100:103], v[80:95]
	v_mfma_f32_32x32x16_bf16 v[64:79], v[188:191], v[100:103], v[64:79]
	ds_read_b128 v[184:187], v218 offset:16512
	ds_read_b128 v[188:191], v218 offset:24704
	s_waitcnt lgkmcnt(8)
	v_mfma_f32_32x32x16_bf16 v[80:95], v[192:195], v[104:107], v[80:95]
	v_mfma_f32_32x32x16_bf16 v[64:79], v[196:199], v[104:107], v[64:79]
	ds_read_b128 v[192:195], v219 offset:16512
	ds_read_b128 v[196:199], v219 offset:24704
	s_waitcnt lgkmcnt(8)
	v_mfma_f32_32x32x16_bf16 v[80:95], v[200:203], v[108:111], v[80:95]
	v_mfma_f32_32x32x16_bf16 v[64:79], v[204:207], v[108:111], v[64:79]
	ds_read_b128 v[200:203], v220 offset:32768
	ds_read_b128 v[204:207], v220 offset:36864
	s_waitcnt lgkmcnt(8)
	v_mfma_f32_32x32x16_bf16 v[80:95], v[208:211], v[112:115], v[80:95]
	v_mfma_f32_32x32x16_bf16 v[64:79], v[212:215], v[112:115], v[64:79]
	ds_read_b128 v[208:211], v221 offset:32768
	ds_read_b128 v[212:215], v221 offset:36864
	s_waitcnt lgkmcnt(8)
	v_mfma_f32_32x32x16_bf16 v[80:95], v[176:179], v[116:119], v[80:95]
	v_mfma_f32_32x32x16_bf16 v[64:79], v[180:183], v[116:119], v[64:79]
	ds_read_b128 v[176:179], v222 offset:32768
	ds_read_b128 v[180:183], v222 offset:36864
	s_waitcnt lgkmcnt(8)
	v_mfma_f32_32x32x16_bf16 v[80:95], v[184:187], v[120:123], v[80:95]
	v_mfma_f32_32x32x16_bf16 v[64:79], v[188:191], v[120:123], v[64:79]
	ds_read_b128 v[184:187], v223 offset:32768
	ds_read_b128 v[188:191], v223 offset:36864
	s_waitcnt lgkmcnt(8)
	v_mfma_f32_32x32x16_bf16 v[80:95], v[192:195], v[96:99], v[80:95]
	v_mfma_f32_32x32x16_bf16 v[64:79], v[196:199], v[96:99], v[64:79]
	s_waitcnt lgkmcnt(6)
	v_mfma_f32_32x32x16_bf16 v[80:95], v[200:203], v[128:131], v[80:95]
	v_mfma_f32_32x32x16_bf16 v[64:79], v[204:207], v[128:131], v[64:79]
	s_waitcnt lgkmcnt(4)
	v_mfma_f32_32x32x16_bf16 v[80:95], v[208:211], v[136:139], v[80:95]
	v_mfma_f32_32x32x16_bf16 v[64:79], v[212:215], v[136:139], v[64:79]
	s_waitcnt lgkmcnt(2)
	v_mfma_f32_32x32x16_bf16 v[80:95], v[176:179], v[132:135], v[80:95]
	v_mfma_f32_32x32x16_bf16 v[64:79], v[180:183], v[132:135], v[64:79]
	s_waitcnt lgkmcnt(0)
	v_mfma_f32_32x32x16_bf16 v[80:95], v[184:187], v[140:143], v[80:95]
	v_mfma_f32_32x32x16_bf16 v[64:79], v[188:191], v[140:143], v[64:79]
	s_setprio 0
	v_add_u32_e32 v252, s72, v171
	ds_read_b64_tr_b16 v[224:225], v252 offset:0
	ds_read_b64_tr_b16 v[226:227], v252 offset:2048
	ds_read_b64_tr_b16 v[228:229], v252 offset:4096
	ds_read_b64_tr_b16 v[230:231], v252 offset:6144
	ds_read_b64_tr_b16 v[232:233], v252 offset:8192
	ds_read_b64_tr_b16 v[234:235], v252 offset:10240
	ds_read_b64_tr_b16 v[236:237], v252 offset:12288
	ds_read_b64_tr_b16 v[238:239], v252 offset:14336
	s_cbranch_scc1 .LBB0_723
; __device__ __forceinline__ void mask_tile(f32x16& p0, f32x16& p1, int dq) {
;     const float NEG = -__builtin_inff();
; #pragma unroll
;     for (int r = 0; r < 16; ++r) { const int c = (r & 3) + 8 * (r >> 2);
;         if (dq - c < 0) p0[r] = NEG;
;         if (dq - c - 32 < 0) p1[r] = NEG; }
; }
	v_cmp_gt_i32_e64 s[62:63], 26, v172
	v_cmp_gt_i32_e64 s[64:65], 27, v172
	v_cmp_gt_i32_e64 s[60:61], 25, v172
	s_and_b64 s[62:63], s[64:65], s[62:63]
	v_cmp_gt_i32_e64 s[58:59], 24, v172
	s_and_b64 s[60:61], s[62:63], s[60:61]
	v_cmp_gt_i32_e64 s[56:57], 19, v172
	s_and_b64 s[58:59], s[60:61], s[58:59]
	v_cmp_gt_i32_e64 s[54:55], 18, v172
	s_and_b64 s[56:57], s[58:59], s[56:57]
	v_cmp_gt_i32_e64 s[52:53], 17, v172
	s_and_b64 s[54:55], s[56:57], s[54:55]
	v_cmp_gt_i32_e64 s[50:51], 16, v172
	s_and_b64 s[52:53], s[54:55], s[52:53]
	v_cmp_gt_i32_e64 s[48:49], 11, v172
	s_and_b64 s[50:51], s[52:53], s[50:51]
	v_cmp_gt_i32_e64 s[46:47], 10, v172
	s_and_b64 s[48:49], s[50:51], s[48:49]
	v_cmp_gt_i32_e64 s[44:45], 9, v172
	s_and_b64 s[46:47], s[48:49], s[46:47]
	v_cmp_gt_i32_e64 s[42:43], 8, v172
	s_and_b64 s[44:45], s[46:47], s[44:45]
	v_cmp_gt_i32_e64 s[40:41], 3, v172
	s_and_b64 s[42:43], s[44:45], s[42:43]
	v_cmp_gt_i32_e64 s[38:39], 2, v172
	s_and_b64 s[40:41], s[42:43], s[40:41]
	v_cmp_gt_i32_e64 s[36:37], 1, v172
	s_and_b64 s[38:39], s[40:41], s[38:39]
	v_cmp_gt_i32_e64 s[34:35], 0, v172
	s_and_b64 s[36:37], s[38:39], s[36:37]
	s_and_b64 s[34:35], s[36:37], s[34:35]
	v_cmp_gt_i32_e64 s[30:31], 58, v172
	v_cndmask_b32_e64 v80, v80, v173, s[34:35]
	v_cmp_gt_i32_e64 s[34:35], 59, v172
	v_cmp_gt_i32_e64 s[28:29], 57, v172
	s_and_b64 s[30:31], s[34:35], s[30:31]
	v_cmp_gt_i32_e64 s[26:27], 56, v172
	s_and_b64 s[28:29], s[30:31], s[28:29]
	v_cmp_gt_i32_e64 s[24:25], 51, v172
	s_and_b64 s[26:27], s[28:29], s[26:27]
	v_cmp_gt_i32_e64 s[22:23], 50, v172
	s_and_b64 s[24:25], s[26:27], s[24:25]
	v_cmp_gt_i32_e64 s[20:21], 49, v172
	s_and_b64 s[22:23], s[24:25], s[22:23]
	v_cmp_gt_i32_e64 s[18:19], 48, v172
	s_and_b64 s[20:21], s[22:23], s[20:21]
	v_cmp_gt_i32_e64 s[16:17], 43, v172
	s_and_b64 s[18:19], s[20:21], s[18:19]
	v_cmp_gt_i32_e64 s[14:15], 42, v172
	s_and_b64 s[16:17], s[18:19], s[16:17]
	v_cmp_gt_i32_e64 s[12:13], 41, v172
	s_and_b64 s[14:15], s[16:17], s[14:15]
	v_cmp_gt_i32_e64 s[10:11], 40, v172
	s_and_b64 s[12:13], s[14:15], s[12:13]
	v_cmp_gt_i32_e64 s[8:9], 35, v172
	s_and_b64 s[10:11], s[12:13], s[10:11]
	v_cmp_gt_i32_e64 s[6:7], 34, v172
	s_and_b64 s[8:9], s[10:11], s[8:9]
	v_cmp_gt_i32_e64 s[4:5], 33, v172
	v_cndmask_b32_e64 v94, v94, v173, s[62:63]
	v_cndmask_b32_e64 v93, v93, v173, s[60:61]
	v_cndmask_b32_e64 v92, v92, v173, s[58:59]
	v_cndmask_b32_e64 v91, v91, v173, s[56:57]
	v_cndmask_b32_e64 v90, v90, v173, s[54:55]
	v_cndmask_b32_e64 v89, v89, v173, s[52:53]
	v_cndmask_b32_e64 v88, v88, v173, s[50:51]
	v_cndmask_b32_e64 v87, v87, v173, s[48:49]
	v_readlane_b32 s48, v254, 42
	s_and_b64 s[6:7], s[8:9], s[6:7]
	v_cmp_gt_i32_e32 vcc, 32, v172
	v_readlane_b32 s52, v254, 46
	v_readlane_b32 s53, v254, 47
	v_readlane_b32 s56, v254, 50
	v_readlane_b32 s57, v254, 51
	v_readlane_b32 s58, v254, 52
	v_readlane_b32 s59, v254, 53
	v_readlane_b32 s60, v254, 54
	v_readlane_b32 s61, v254, 55
	s_and_b64 s[4:5], s[6:7], s[4:5]
	v_readlane_b32 s62, v254, 56
	v_readlane_b32 s63, v254, 57
	s_mov_b64 s[52:53], s[56:57]
	s_mov_b64 s[56:57], s[60:61]
	s_and_b64 vcc, s[4:5], vcc
	v_cndmask_b32_e64 v95, v95, v173, s[64:65]
	s_mov_b64 s[58:59], s[62:63]
	v_cndmask_b32_e64 v86, v86, v173, s[46:47]
	v_cndmask_b32_e64 v85, v85, v173, s[44:45]
	v_cndmask_b32_e64 v84, v84, v173, s[42:43]
	v_cndmask_b32_e64 v83, v83, v173, s[40:41]
	v_cndmask_b32_e64 v82, v82, v173, s[38:39]
	v_cndmask_b32_e64 v81, v81, v173, s[36:37]
	v_cndmask_b32_e64 v79, v79, v173, s[34:35]
	v_cndmask_b32_e64 v78, v78, v173, s[30:31]
	v_cndmask_b32_e64 v77, v77, v173, s[28:29]
	v_cndmask_b32_e64 v76, v76, v173, s[26:27]
	v_cndmask_b32_e64 v75, v75, v173, s[24:25]
	v_cndmask_b32_e64 v74, v74, v173, s[22:23]
	v_cndmask_b32_e64 v73, v73, v173, s[20:21]
	v_cndmask_b32_e64 v72, v72, v173, s[18:19]
	v_cndmask_b32_e64 v71, v71, v173, s[16:17]
	v_cndmask_b32_e64 v70, v70, v173, s[14:15]
	v_cndmask_b32_e64 v69, v69, v173, s[12:13]
	v_cndmask_b32_e64 v68, v68, v173, s[10:11]
	v_cndmask_b32_e64 v67, v67, v173, s[8:9]
	v_cndmask_b32_e64 v66, v66, v173, s[6:7]
	v_cndmask_b32_e64 v65, v65, v173, s[4:5]
	v_cndmask_b32_e32 v64, v64, v173, vcc
	v_readlane_b32 s49, v254, 43
	v_readlane_b32 s50, v254, 44
	v_readlane_b32 s51, v254, 45
	v_readlane_b32 s54, v254, 48
	v_readlane_b32 s55, v254, 49

; __device__ __forceinline__ void partialSM(f32x16& p0, f32x16& p1, float& m_reg, float& mn, float& alpha) {
;     float pmax = p0[0];
; #pragma unroll
;     for (int r = 1; r < 16; ++r) pmax = fmaxf(pmax, p0[r]);
; #pragma unroll
;     for (int r = 0; r < 16; ++r) pmax = fmaxf(pmax, p1[r]);
;     { auto rr = __builtin_amdgcn_permlane32_swap(__float_as_uint(pmax), __float_as_uint(pmax), false, false);
;       pmax = fmaxf(__uint_as_float(rr[0]), __uint_as_float(rr[1])); }
;     mn = fmaxf(m_reg, pmax); alpha = __builtin_amdgcn_exp2f((m_reg - mn) * C2); m_reg = mn;
;     const float mnL = -mn * C2;
; #pragma unroll
;     for (int r = 0; r < 16; ++r) p0[r] = __builtin_amdgcn_exp2f(fmaf(p0[r], C2, mnL));
; #pragma unroll
;     for (int r = 0; r < 16; ++r) p1[r] = __builtin_amdgcn_exp2f(fmaf(p1[r], C2, mnL));
; }
; __device__ __forceinline__ void finishSM(f32x16& p0, f32x16& p1, float alpha, float& l_reg, bf16x8& pa0, bf16x8& pa1, bf16x8& pa2, bf16x8& pa3) {
;     float ps = 0;
; #pragma unroll
;     for (int r = 0; r < 16; ++r) ps += p0[r];
; #pragma unroll
;     for (int r = 0; r < 16; ++r) ps += p1[r];
;     { auto rr = __builtin_amdgcn_permlane32_swap(__float_as_uint(ps), __float_as_uint(ps), false, false);
;       ps = __uint_as_float(rr[0]) + __uint_as_float(rr[1]); }
;     l_reg = l_reg * alpha + ps;
;     ...
;     PK4(p0, 0, pa0); PK4(p0, 8, pa1); PK4(p1, 0, pa2); PK4(p1, 8, pa3);
; __device__ __forceinline__ void pv_tile(f32x16* o, int vb0  , bf16x8 pa0, bf16x8 pa1, bf16x8 pa2, bf16x8 pa3) {
;     ...
;     PV_D0(0); PV_D0(1); PV_D0(2); PV_D0(3);
.LBB0_727:
	v_mul_f32_e32 v176, 0xbdd53b94, v174
	v_fmamk_f32 v64, v64, 0x3dd53b94, v176
	v_exp_f32_e32 v177, v64
	v_fmamk_f32 v64, v65, 0x3dd53b94, v176
	v_exp_f32_e32 v178, v64
	v_fmamk_f32 v64, v66, 0x3dd53b94, v176
	v_exp_f32_e32 v179, v64
	v_fmamk_f32 v64, v67, 0x3dd53b94, v176
	v_exp_f32_e32 v180, v64
	v_fmamk_f32 v64, v68, 0x3dd53b94, v176
	v_exp_f32_e32 v181, v64
	v_fmamk_f32 v64, v69, 0x3dd53b94, v176
	v_exp_f32_e32 v182, v64
	v_fmamk_f32 v64, v70, 0x3dd53b94, v176
	v_exp_f32_e32 v183, v64
	v_fmamk_f32 v64, v71, 0x3dd53b94, v176
	v_exp_f32_e32 v184, v64
	v_fmamk_f32 v64, v72, 0x3dd53b94, v176
	v_exp_f32_e32 v185, v64
	v_fmamk_f32 v64, v73, 0x3dd53b94, v176
	v_fmamk_f32 v80, v80, 0x3dd53b94, v176
	v_exp_f32_e32 v186, v64
	v_fmamk_f32 v64, v74, 0x3dd53b94, v176
	v_exp_f32_e32 v80, v80
	v_fmamk_f32 v81, v81, 0x3dd53b94, v176
	v_exp_f32_e32 v187, v64
	v_fmamk_f32 v64, v75, 0x3dd53b94, v176
	v_exp_f32_e32 v81, v81
	v_fmamk_f32 v82, v82, 0x3dd53b94, v176
	v_exp_f32_e32 v188, v64
	v_fmamk_f32 v64, v76, 0x3dd53b94, v176
	v_exp_f32_e32 v82, v82
	v_fmamk_f32 v83, v83, 0x3dd53b94, v176
	v_exp_f32_e32 v189, v64
	v_fmamk_f32 v64, v77, 0x3dd53b94, v176
	v_exp_f32_e32 v83, v83
	v_fmamk_f32 v84, v84, 0x3dd53b94, v176
	v_exp_f32_e32 v190, v64
	v_fmamk_f32 v64, v78, 0x3dd53b94, v176
	v_exp_f32_e32 v84, v84
	v_fmamk_f32 v85, v85, 0x3dd53b94, v176
	v_exp_f32_e32 v191, v64
	v_add_f32_e32 v64, 0, v80
	v_exp_f32_e32 v85, v85
	v_fmamk_f32 v86, v86, 0x3dd53b94, v176
	v_add_f32_e32 v64, v81, v64
	v_exp_f32_e32 v86, v86
	v_fmamk_f32 v87, v87, 0x3dd53b94, v176
	v_add_f32_e32 v64, v82, v64
	v_exp_f32_e32 v87, v87
	v_fmamk_f32 v88, v88, 0x3dd53b94, v176
	v_add_f32_e32 v64, v83, v64
	v_exp_f32_e32 v88, v88
	v_fmamk_f32 v89, v89, 0x3dd53b94, v176
	v_add_f32_e32 v64, v84, v64
	v_exp_f32_e32 v89, v89
	v_fmamk_f32 v90, v90, 0x3dd53b94, v176
	v_add_f32_e32 v64, v85, v64
	v_exp_f32_e32 v90, v90
	v_fmamk_f32 v91, v91, 0x3dd53b94, v176
	v_add_f32_e32 v64, v86, v64
	v_exp_f32_e32 v91, v91
	v_fmamk_f32 v92, v92, 0x3dd53b94, v176
	v_add_f32_e32 v64, v87, v64
	v_exp_f32_e32 v92, v92
	v_fmamk_f32 v93, v93, 0x3dd53b94, v176
	v_add_f32_e32 v64, v88, v64
	v_exp_f32_e32 v93, v93
	v_fmamk_f32 v94, v94, 0x3dd53b94, v176
	v_add_f32_e32 v64, v89, v64
	v_exp_f32_e32 v94, v94
	v_fmamk_f32 v95, v95, 0x3dd53b94, v176
	v_add_f32_e32 v64, v90, v64
	v_exp_f32_e32 v95, v95
	v_add_f32_e32 v64, v91, v64
	v_add_f32_e32 v64, v92, v64
	v_add_f32_e32 v64, v93, v64
	v_add_f32_e32 v64, v94, v64
	v_add_f32_e32 v64, v95, v64
	v_add_f32_e32 v64, v177, v64
	v_add_f32_e32 v64, v178, v64
	v_add_f32_e32 v64, v179, v64
	v_add_f32_e32 v64, v180, v64
	v_add_f32_e32 v64, v181, v64
	v_add_f32_e32 v64, v182, v64
	v_add_f32_e32 v64, v183, v64
	v_add_f32_e32 v64, v184, v64
	v_add_f32_e32 v64, v185, v64
	v_add_f32_e32 v64, v186, v64
	v_fmac_f32_e32 v176, 0x3dd53b94, v79
	v_add_f32_e32 v64, v187, v64
	v_exp_f32_e32 v79, v176
	v_add_f32_e32 v64, v188, v64
	v_add_f32_e32 v64, v189, v64
	v_add_f32_e32 v64, v190, v64
	v_add_f32_e32 v64, v191, v64
	v_add_f32_e32 v64, v79, v64
	v_mov_b32_e32 v65, v64
	s_nop 1
	v_permlane32_swap_b32_e32 v64, v65
	v_add_f32_e32 v192, v64, v65
	v_cvt_pk_bf16_f32 v64, v80, v81
	v_cvt_pk_bf16_f32 v65, v82, v83
	v_cvt_pk_bf16_f32 v66, v84, v85
	v_cvt_pk_bf16_f32 v67, v86, v87
	v_cvt_pk_bf16_f32 v68, v88, v89
	v_cvt_pk_bf16_f32 v69, v90, v91
	v_cvt_pk_bf16_f32 v70, v92, v93
	v_cvt_pk_bf16_f32 v71, v94, v95
	v_cvt_pk_bf16_f32 v72, v177, v178
	v_cvt_pk_bf16_f32 v73, v179, v180
	v_cvt_pk_bf16_f32 v74, v181, v182
	v_cvt_pk_bf16_f32 v75, v183, v184
	v_cvt_pk_bf16_f32 v76, v185, v186
	v_cvt_pk_bf16_f32 v77, v187, v188
	v_cvt_pk_bf16_f32 v78, v189, v190
	v_cvt_pk_bf16_f32 v79, v191, v79
	v_fmac_f32_e32 v192, v145, v175
	v_permlane32_swap_b32_e32 v64, v66
	v_permlane32_swap_b32_e32 v65, v67
	v_permlane32_swap_b32_e32 v68, v70
	v_permlane32_swap_b32_e32 v69, v71
	v_permlane32_swap_b32_e32 v72, v74
	v_permlane32_swap_b32_e32 v73, v75
	v_permlane32_swap_b32_e32 v76, v78
	v_permlane32_swap_b32_e32 v77, v79
	ds_read_b64_tr_b16 v[80:81], v252 offset:512
	ds_read_b64_tr_b16 v[82:83], v252 offset:2560
	ds_read_b64_tr_b16 v[84:85], v252 offset:4608
	ds_read_b64_tr_b16 v[86:87], v252 offset:6656
	ds_read_b64_tr_b16 v[88:89], v252 offset:8704
	ds_read_b64_tr_b16 v[90:91], v252 offset:10752
	ds_read_b64_tr_b16 v[92:93], v252 offset:12800
	ds_read_b64_tr_b16 v[94:95], v252 offset:14848
	s_waitcnt lgkmcnt(8)
	s_setprio 1
	v_mfma_f32_32x32x16_bf16 v[48:63], v[64:67], v[224:227], v[48:63]
	v_mfma_f32_32x32x16_bf16 v[48:63], v[68:71], v[228:231], v[48:63]
	v_mfma_f32_32x32x16_bf16 v[48:63], v[72:75], v[232:235], v[48:63]
	v_mfma_f32_32x32x16_bf16 v[48:63], v[76:79], v[236:239], v[48:63]
	ds_read_b64_tr_b16 v[224:225], v252 offset:1024
	ds_read_b64_tr_b16 v[226:227], v252 offset:3072
	ds_read_b64_tr_b16 v[228:229], v252 offset:5120
	ds_read_b64_tr_b16 v[230:231], v252 offset:7168
	ds_read_b64_tr_b16 v[232:233], v252 offset:9216
	ds_read_b64_tr_b16 v[234:235], v252 offset:11264
	ds_read_b64_tr_b16 v[236:237], v252 offset:13312
	ds_read_b64_tr_b16 v[238:239], v252 offset:15360
	s_waitcnt lgkmcnt(8)
	v_mfma_f32_32x32x16_bf16 v[32:47], v[64:67], v[80:83], v[32:47]
	v_mfma_f32_32x32x16_bf16 v[32:47], v[68:71], v[84:87], v[32:47]
	v_mfma_f32_32x32x16_bf16 v[32:47], v[72:75], v[88:91], v[32:47]
	v_mfma_f32_32x32x16_bf16 v[32:47], v[76:79], v[92:95], v[32:47]
	ds_read_b64_tr_b16 v[80:81], v252 offset:1536
	ds_read_b64_tr_b16 v[82:83], v252 offset:3584
	ds_read_b64_tr_b16 v[84:85], v252 offset:5632
	ds_read_b64_tr_b16 v[86:87], v252 offset:7680
	ds_read_b64_tr_b16 v[88:89], v252 offset:9728
	ds_read_b64_tr_b16 v[90:91], v252 offset:11776
	ds_read_b64_tr_b16 v[92:93], v252 offset:13824
	ds_read_b64_tr_b16 v[94:95], v252 offset:15872
	s_waitcnt lgkmcnt(8)
	v_mfma_f32_32x32x16_bf16 v[16:31], v[64:67], v[224:227], v[16:31]
	v_mfma_f32_32x32x16_bf16 v[16:31], v[68:71], v[228:231], v[16:31]
	v_mfma_f32_32x32x16_bf16 v[16:31], v[72:75], v[232:235], v[16:31]
	v_mfma_f32_32x32x16_bf16 v[16:31], v[76:79], v[236:239], v[16:31]
	s_waitcnt lgkmcnt(0)
	v_mov_b32_e32 v145, v192
	v_mfma_f32_32x32x16_bf16 v[0:15], v[64:67], v[80:83], v[0:15]
	v_mfma_f32_32x32x16_bf16 v[0:15], v[68:71], v[84:87], v[0:15]
	v_mfma_f32_32x32x16_bf16 v[0:15], v[72:75], v[88:91], v[0:15]
	v_mfma_f32_32x32x16_bf16 v[0:15], v[76:79], v[92:95], v[0:15]
	s_setprio 0
	s_branch .LBB0_729
